# on top of the previous stack: the 8 permlane swaps of the P pack moved behind the 16 V-fragment LDS reads in both wave halves of the diff-attention tail
# speedup vs baseline: 1.0038x; 1.0017x over previous
.LBB0_719:
	v_cvt_pk_bf16_f32 v96, v123, v127
	v_cvt_pk_bf16_f32 v97, v124, v126
	v_cvt_pk_bf16_f32 v98, v125, v129
	v_cvt_pk_bf16_f32 v99, v122, v128
	v_cvt_pk_bf16_f32 v92, v89, v91
	v_cvt_pk_bf16_f32 v93, v88, v90
	v_cvt_pk_bf16_f32 v94, v107, v109
	v_cvt_pk_bf16_f32 v95, v106, v108
	v_cvt_pk_bf16_f32 v88, v117, v119
	v_cvt_pk_bf16_f32 v89, v84, v118
	v_cvt_pk_bf16_f32 v90, v85, v121
	v_cvt_pk_bf16_f32 v91, v116, v120
	v_cvt_pk_bf16_f32 v84, v87, v101
	v_cvt_pk_bf16_f32 v85, v86, v100
	v_cvt_pk_bf16_f32 v86, v103, v105
	v_cvt_pk_bf16_f32 v87, v102, v104
	v_cndmask_b32_e64 v1, 0, 1, s[58:59]
	v_cmp_ne_u32_e64 s[10:11], 1, v1
	s_andn2_b64 vcc, exec, s[58:59]
	s_cbranch_vccnz .Lm1_pre
	v_add_u32_e32 v1, s2, v222
	ds_read_b64_tr_b16 v[100:101], v1 offset:0
	ds_read_b64_tr_b16 v[102:103], v1 offset:0x800
	ds_read_b64_tr_b16 v[104:105], v1 offset:0x1000
	ds_read_b64_tr_b16 v[106:107], v1 offset:0x1800
	ds_read_b64_tr_b16 v[108:109], v1 offset:0x2000
	ds_read_b64_tr_b16 v[110:111], v1 offset:0x2800
	ds_read_b64_tr_b16 v[112:113], v1 offset:0x3000
	ds_read_b64_tr_b16 v[114:115], v1 offset:0x3800
	ds_read_b64_tr_b16 v[116:117], v1 offset:0x200
	ds_read_b64_tr_b16 v[118:119], v1 offset:0xa00
	ds_read_b64_tr_b16 v[120:121], v1 offset:0x1200
	ds_read_b64_tr_b16 v[122:123], v1 offset:0x1a00
	ds_read_b64_tr_b16 v[124:125], v1 offset:0x2200
	ds_read_b64_tr_b16 v[126:127], v1 offset:0x2a00
	ds_read_b64_tr_b16 v[128:129], v1 offset:0x3200
	ds_read_b64_tr_b16 v[130:131], v1 offset:0x3a00
	v_permlane32_swap_b32_e32 v96, v98
	v_permlane32_swap_b32_e32 v97, v99
	v_permlane32_swap_b32_e32 v92, v94
	v_permlane32_swap_b32_e32 v93, v95
	v_permlane32_swap_b32_e32 v88, v90
	v_permlane32_swap_b32_e32 v89, v91
	v_permlane32_swap_b32_e32 v84, v86
	v_permlane32_swap_b32_e32 v85, v87
	s_nop 1
	s_waitcnt lgkmcnt(8)
	s_nop 0
	v_mfma_f32_32x32x16_bf16 v[52:67], v[96:99], v[100:103], v[52:67]
	v_mfma_f32_32x32x16_bf16 v[52:67], v[92:95], v[104:107], v[52:67]
	v_mfma_f32_32x32x16_bf16 v[52:67], v[88:91], v[108:111], v[52:67]
	v_mfma_f32_32x32x16_bf16 v[52:67], v[84:87], v[112:115], v[52:67]
	ds_read_b64_tr_b16 v[100:101], v1 offset:0x400
	ds_read_b64_tr_b16 v[102:103], v1 offset:0xc00
	ds_read_b64_tr_b16 v[104:105], v1 offset:0x1400
	ds_read_b64_tr_b16 v[106:107], v1 offset:0x1c00
	ds_read_b64_tr_b16 v[108:109], v1 offset:0x2400
	ds_read_b64_tr_b16 v[110:111], v1 offset:0x2c00
	ds_read_b64_tr_b16 v[112:113], v1 offset:0x3400
	ds_read_b64_tr_b16 v[114:115], v1 offset:0x3c00
	s_waitcnt lgkmcnt(8)
	v_mfma_f32_32x32x16_bf16 v[36:51], v[96:99], v[116:119], v[36:51]
	v_mfma_f32_32x32x16_bf16 v[36:51], v[92:95], v[120:123], v[36:51]
	v_mfma_f32_32x32x16_bf16 v[36:51], v[88:91], v[124:127], v[36:51]
	v_mfma_f32_32x32x16_bf16 v[36:51], v[84:87], v[128:131], v[36:51]
	ds_read_b64_tr_b16 v[116:117], v1 offset:0x600
	ds_read_b64_tr_b16 v[118:119], v1 offset:0xe00
	ds_read_b64_tr_b16 v[120:121], v1 offset:0x1600
	ds_read_b64_tr_b16 v[122:123], v1 offset:0x1e00
	ds_read_b64_tr_b16 v[124:125], v1 offset:0x2600
	ds_read_b64_tr_b16 v[126:127], v1 offset:0x2e00
	ds_read_b64_tr_b16 v[128:129], v1 offset:0x3600
	ds_read_b64_tr_b16 v[130:131], v1 offset:0x3e00
	s_waitcnt lgkmcnt(8)
	v_mfma_f32_32x32x16_bf16 v[20:35], v[96:99], v[100:103], v[20:35]
	v_mfma_f32_32x32x16_bf16 v[20:35], v[92:95], v[104:107], v[20:35]
	v_mfma_f32_32x32x16_bf16 v[20:35], v[88:91], v[108:111], v[20:35]
	v_mfma_f32_32x32x16_bf16 v[20:35], v[84:87], v[112:115], v[20:35]
	s_waitcnt lgkmcnt(0)
	v_mfma_f32_32x32x16_bf16 v[4:19], v[96:99], v[116:119], v[4:19]
	v_mfma_f32_32x32x16_bf16 v[4:19], v[92:95], v[120:123], v[4:19]
	v_mfma_f32_32x32x16_bf16 v[4:19], v[88:91], v[124:127], v[4:19]
	v_mfma_f32_32x32x16_bf16 v[4:19], v[84:87], v[128:131], v[4:19]
	s_branch .LBB0_635
.Lm1_pre:
	s_add_i32 s0, s4, 0x10000
	s_and_b32 s0, s0, 0x18000
	v_add_u32_e32 v1, s0, v222
	ds_read_b64_tr_b16 v[100:101], v1 offset:0
	ds_read_b64_tr_b16 v[102:103], v1 offset:0x800
	ds_read_b64_tr_b16 v[104:105], v1 offset:0x1000
	ds_read_b64_tr_b16 v[106:107], v1 offset:0x1800
	ds_read_b64_tr_b16 v[108:109], v1 offset:0x2000
	ds_read_b64_tr_b16 v[110:111], v1 offset:0x2800
	ds_read_b64_tr_b16 v[112:113], v1 offset:0x3000
	ds_read_b64_tr_b16 v[114:115], v1 offset:0x3800
	ds_read_b64_tr_b16 v[116:117], v1 offset:0x200
	ds_read_b64_tr_b16 v[118:119], v1 offset:0xa00
	ds_read_b64_tr_b16 v[120:121], v1 offset:0x1200
	ds_read_b64_tr_b16 v[122:123], v1 offset:0x1a00
	ds_read_b64_tr_b16 v[124:125], v1 offset:0x2200
	ds_read_b64_tr_b16 v[126:127], v1 offset:0x2a00
	ds_read_b64_tr_b16 v[128:129], v1 offset:0x3200
	ds_read_b64_tr_b16 v[130:131], v1 offset:0x3a00
	v_permlane32_swap_b32_e32 v96, v98
	v_permlane32_swap_b32_e32 v97, v99
	v_permlane32_swap_b32_e32 v92, v94
	v_permlane32_swap_b32_e32 v93, v95
	v_permlane32_swap_b32_e32 v88, v90
	v_permlane32_swap_b32_e32 v89, v91
	v_permlane32_swap_b32_e32 v84, v86
	v_permlane32_swap_b32_e32 v85, v87
	s_branch .LBB0_635
